# bf16 GEMM epilogues (in-proj, out-proj): lane transpose via ds_bpermute so 4 consecutive lanes store one row's 64 contiguous bytes (on top of conversion routine)
# speedup vs baseline: 1.0128x; 1.0034x over previous
.LBB0_185:
	v_mbcnt_lo_u32_b32 v254, -1, 0
	v_mbcnt_hi_u32_b32 v254, -1, v254
	v_lshrrev_b32_e32 v253, 2, v254
	v_add_u32_e32 v253, v253, v163
	v_and_b32_e32 v254, 15, v254
	v_sub_u32_e32 v253, v253, v254
	v_lshl_add_u32 v192, s88, 8, v253
	v_mbcnt_lo_u32_b32 v254, -1, 0
	v_mbcnt_hi_u32_b32 v254, -1, v254
	v_lshrrev_b32_e32 v253, 4, v254
	v_lshlrev_b32_e32 v253, 3, v253
	v_sub_u32_e32 v253, v181, v253
	v_and_b32_e32 v254, 3, v254
	v_lshl_add_u32 v253, v254, 3, v253
	v_lshl_or_b32 v160, s89, 8, v253
	v_mbcnt_lo_u32_b32 v254, -1, 0
	v_mbcnt_hi_u32_b32 v254, -1, v254
	v_lshrrev_b32_e32 v253, 2, v254
	v_lshlrev_b32_e32 v253, 2, v253
	v_and_b32_e32 v254, 3, v254
	v_lshl_or_b32 v253, v254, 6, v253
	s_lshl_b32 s39, s10, 10
	s_and_b32 s39, s39, 0x400
	v_add_u32_e32 v130, s39, v164
	ds_read_b128 v[142:145], v130
	ds_read_b128 v[138:141], v130 offset:16
	ds_read_b128 v[134:137], v130 offset:512
	ds_read_b128 v[130:133], v130 offset:528
	s_and_b32 s40, s89, -4
	s_cmp_eq_u32 s40, 12
	s_cselect_b64 vcc, -1, 0
	v_ashrrev_i32_e32 v161, 31, v160
	v_mov_b64_e32 v[158:159], s[26:27]
	v_cndmask_b32_e32 v150, 1.0, v183, vcc
	v_mad_i64_i32 v[188:189], s[40:41], v192, s76, v[158:159]
	v_lshlrev_b64 v[160:161], 1, v[160:161]
	s_waitcnt lgkmcnt(0)
	v_pk_add_f32 v[128:129], v[128:129], v[144:145]
	v_pk_add_f32 v[126:127], v[126:127], v[142:143]
	v_pk_add_f32 v[124:125], v[124:125], v[140:141]
	v_pk_add_f32 v[122:123], v[122:123], v[138:139]
	v_lshl_add_u64 v[188:189], v[188:189], 0, v[160:161]
	v_pk_mul_f32 v[128:129], v[150:151], v[128:129] op_sel_hi:[0,1]
	v_pk_mul_f32 v[126:127], v[150:151], v[126:127] op_sel_hi:[0,1]
	v_pk_mul_f32 v[190:191], v[150:151], v[124:125] op_sel_hi:[0,1]
	v_pk_mul_f32 v[124:125], v[150:151], v[122:123] op_sel_hi:[0,1]
	v_cvt_pk_bf16_f32 v122, v126, v127
	v_cvt_pk_bf16_f32 v123, v128, v129
	v_pk_add_f32 v[118:119], v[118:119], v[134:135]
	v_pk_add_f32 v[112:113], v[112:113], v[132:133]
	v_pk_add_f32 v[110:111], v[110:111], v[130:131]
	v_cvt_pk_bf16_f32 v124, v124, v125
	v_cvt_pk_bf16_f32 v125, v190, v191
	ds_bpermute_b32 v122, v253, v122
	ds_bpermute_b32 v123, v253, v123
	ds_bpermute_b32 v124, v253, v124
	ds_bpermute_b32 v125, v253, v125
	s_waitcnt lgkmcnt(0)
	global_store_dwordx4 v[188:189], v[122:125], off
	v_pk_add_f32 v[120:121], v[120:121], v[136:137]
	v_pk_mul_f32 v[118:119], v[150:151], v[118:119] op_sel_hi:[0,1]
	v_pk_mul_f32 v[122:123], v[150:151], v[112:113] op_sel_hi:[0,1]
	v_pk_mul_f32 v[112:113], v[150:151], v[110:111] op_sel_hi:[0,1]
	v_cvt_pk_bf16_f32 v110, v118, v119
	v_pk_mul_f32 v[120:121], v[150:151], v[120:121] op_sel_hi:[0,1]
	v_cvt_pk_bf16_f32 v111, v120, v121
	v_cvt_pk_bf16_f32 v112, v112, v113
	v_cvt_pk_bf16_f32 v113, v122, v123
	ds_bpermute_b32 v110, v253, v110
	ds_bpermute_b32 v111, v253, v111
	ds_bpermute_b32 v112, v253, v112
	ds_bpermute_b32 v113, v253, v113
	s_waitcnt lgkmcnt(0)
	global_store_dwordx4 v[188:189], v[110:113], off offset:256
	v_pk_add_f32 v[114:115], v[114:115], v[142:143]
	v_pk_add_f32 v[108:109], v[108:109], v[140:141]
	v_or_b32_e32 v110, 16, v192
	v_mad_i64_i32 v[110:111], s[40:41], v110, s76, v[158:159]
	v_pk_add_f32 v[112:113], v[116:117], v[144:145]
	v_pk_add_f32 v[106:107], v[106:107], v[138:139]
	v_lshl_add_u64 v[110:111], v[110:111], 0, v[160:161]
	v_pk_mul_f32 v[112:113], v[150:151], v[112:113] op_sel_hi:[0,1]
	v_pk_mul_f32 v[114:115], v[150:151], v[114:115] op_sel_hi:[0,1]
	v_pk_mul_f32 v[116:117], v[150:151], v[108:109] op_sel_hi:[0,1]
	v_pk_mul_f32 v[108:109], v[150:151], v[106:107] op_sel_hi:[0,1]
	v_cvt_pk_bf16_f32 v106, v114, v115
	v_cvt_pk_bf16_f32 v107, v112, v113
	v_pk_add_f32 v[102:103], v[102:103], v[134:135]
	v_pk_add_f32 v[96:97], v[96:97], v[132:133]
	v_pk_add_f32 v[94:95], v[94:95], v[130:131]
	v_cvt_pk_bf16_f32 v108, v108, v109
	v_cvt_pk_bf16_f32 v109, v116, v117
	ds_bpermute_b32 v106, v253, v106
	ds_bpermute_b32 v107, v253, v107
	ds_bpermute_b32 v108, v253, v108
	ds_bpermute_b32 v109, v253, v109
	s_waitcnt lgkmcnt(0)
	global_store_dwordx4 v[110:111], v[106:109], off
	v_pk_add_f32 v[104:105], v[104:105], v[136:137]
	v_pk_mul_f32 v[102:103], v[150:151], v[102:103] op_sel_hi:[0,1]
	v_pk_mul_f32 v[106:107], v[150:151], v[96:97] op_sel_hi:[0,1]
	v_pk_mul_f32 v[96:97], v[150:151], v[94:95] op_sel_hi:[0,1]
	v_cvt_pk_bf16_f32 v94, v102, v103
	v_pk_mul_f32 v[104:105], v[150:151], v[104:105] op_sel_hi:[0,1]
	v_cvt_pk_bf16_f32 v95, v104, v105
	v_cvt_pk_bf16_f32 v96, v96, v97
	v_cvt_pk_bf16_f32 v97, v106, v107
	ds_bpermute_b32 v94, v253, v94
	ds_bpermute_b32 v95, v253, v95
	ds_bpermute_b32 v96, v253, v96
	ds_bpermute_b32 v97, v253, v97
	s_waitcnt lgkmcnt(0)
	global_store_dwordx4 v[110:111], v[94:97], off offset:256
	v_pk_add_f32 v[98:99], v[98:99], v[142:143]
	v_pk_add_f32 v[92:93], v[92:93], v[140:141]
	v_or_b32_e32 v94, 32, v192
	v_mad_i64_i32 v[94:95], s[40:41], v94, s76, v[158:159]
	v_pk_add_f32 v[96:97], v[100:101], v[144:145]
	v_pk_add_f32 v[90:91], v[90:91], v[138:139]
	v_lshl_add_u64 v[94:95], v[94:95], 0, v[160:161]
	v_pk_mul_f32 v[96:97], v[150:151], v[96:97] op_sel_hi:[0,1]
	v_pk_mul_f32 v[98:99], v[150:151], v[98:99] op_sel_hi:[0,1]
	v_pk_mul_f32 v[100:101], v[150:151], v[92:93] op_sel_hi:[0,1]
	v_pk_mul_f32 v[92:93], v[150:151], v[90:91] op_sel_hi:[0,1]
	v_cvt_pk_bf16_f32 v90, v98, v99
	v_cvt_pk_bf16_f32 v91, v96, v97
	v_pk_add_f32 v[86:87], v[86:87], v[134:135]
	v_pk_add_f32 v[80:81], v[80:81], v[132:133]
	v_pk_add_f32 v[78:79], v[78:79], v[130:131]
	v_cvt_pk_bf16_f32 v92, v92, v93
	v_cvt_pk_bf16_f32 v93, v100, v101
	ds_bpermute_b32 v90, v253, v90
	ds_bpermute_b32 v91, v253, v91
	ds_bpermute_b32 v92, v253, v92
	ds_bpermute_b32 v93, v253, v93
	s_waitcnt lgkmcnt(0)
	global_store_dwordx4 v[94:95], v[90:93], off
	v_pk_add_f32 v[88:89], v[88:89], v[136:137]
	v_pk_mul_f32 v[86:87], v[150:151], v[86:87] op_sel_hi:[0,1]
	v_pk_mul_f32 v[90:91], v[150:151], v[80:81] op_sel_hi:[0,1]
	v_pk_mul_f32 v[80:81], v[150:151], v[78:79] op_sel_hi:[0,1]
	v_cvt_pk_bf16_f32 v78, v86, v87
	v_pk_mul_f32 v[88:89], v[150:151], v[88:89] op_sel_hi:[0,1]
	v_cvt_pk_bf16_f32 v79, v88, v89
	v_cvt_pk_bf16_f32 v80, v80, v81
	v_cvt_pk_bf16_f32 v81, v90, v91
	ds_bpermute_b32 v78, v253, v78
	ds_bpermute_b32 v79, v253, v79
	ds_bpermute_b32 v80, v253, v80
	ds_bpermute_b32 v81, v253, v81
	s_waitcnt lgkmcnt(0)
	global_store_dwordx4 v[94:95], v[78:81], off offset:256
	v_pk_add_f32 v[82:83], v[82:83], v[142:143]
	v_pk_add_f32 v[76:77], v[76:77], v[140:141]
	v_or_b32_e32 v78, 48, v192
	v_mad_i64_i32 v[78:79], s[40:41], v78, s76, v[158:159]
	v_pk_add_f32 v[80:81], v[84:85], v[144:145]
	v_pk_add_f32 v[74:75], v[74:75], v[138:139]
	v_lshl_add_u64 v[78:79], v[78:79], 0, v[160:161]
	v_pk_mul_f32 v[80:81], v[150:151], v[80:81] op_sel_hi:[0,1]
	v_pk_mul_f32 v[82:83], v[150:151], v[82:83] op_sel_hi:[0,1]
	v_pk_mul_f32 v[84:85], v[150:151], v[76:77] op_sel_hi:[0,1]
	v_pk_mul_f32 v[76:77], v[150:151], v[74:75] op_sel_hi:[0,1]
	v_cvt_pk_bf16_f32 v74, v82, v83
	v_cvt_pk_bf16_f32 v75, v80, v81
	v_pk_add_f32 v[70:71], v[70:71], v[134:135]
	v_pk_add_f32 v[68:69], v[68:69], v[132:133]
	v_pk_add_f32 v[66:67], v[66:67], v[130:131]
	v_cvt_pk_bf16_f32 v76, v76, v77
	v_cvt_pk_bf16_f32 v77, v84, v85
	ds_bpermute_b32 v74, v253, v74
	ds_bpermute_b32 v75, v253, v75
	ds_bpermute_b32 v76, v253, v76
	ds_bpermute_b32 v77, v253, v77
	s_waitcnt lgkmcnt(0)
	global_store_dwordx4 v[78:79], v[74:77], off
	v_pk_add_f32 v[72:73], v[72:73], v[136:137]
	v_pk_mul_f32 v[70:71], v[150:151], v[70:71] op_sel_hi:[0,1]
	v_pk_mul_f32 v[74:75], v[150:151], v[68:69] op_sel_hi:[0,1]
	v_pk_mul_f32 v[68:69], v[150:151], v[66:67] op_sel_hi:[0,1]
	v_cvt_pk_bf16_f32 v66, v70, v71
	v_pk_mul_f32 v[72:73], v[150:151], v[72:73] op_sel_hi:[0,1]
	v_cvt_pk_bf16_f32 v67, v72, v73
	v_cvt_pk_bf16_f32 v68, v68, v69
	v_cvt_pk_bf16_f32 v69, v74, v75
	ds_bpermute_b32 v66, v253, v66
	ds_bpermute_b32 v67, v253, v67
	ds_bpermute_b32 v68, v253, v68
	ds_bpermute_b32 v69, v253, v69
	s_waitcnt lgkmcnt(0)
	global_store_dwordx4 v[78:79], v[66:69], off offset:256
	v_pk_add_f32 v[64:65], v[64:65], v[144:145]
	v_pk_add_f32 v[62:63], v[62:63], v[142:143]
	v_add_u32_e32 v66, 0x80, v192
	v_mad_i64_i32 v[66:67], s[40:41], v66, s76, v[158:159]
	v_pk_add_f32 v[60:61], v[60:61], v[140:141]
	v_pk_add_f32 v[58:59], v[58:59], v[138:139]
	v_lshl_add_u64 v[66:67], v[66:67], 0, v[160:161]
	v_pk_mul_f32 v[64:65], v[150:151], v[64:65] op_sel_hi:[0,1]
	v_pk_mul_f32 v[62:63], v[150:151], v[62:63] op_sel_hi:[0,1]
	v_pk_mul_f32 v[68:69], v[150:151], v[60:61] op_sel_hi:[0,1]
	v_pk_mul_f32 v[60:61], v[150:151], v[58:59] op_sel_hi:[0,1]
	v_cvt_pk_bf16_f32 v58, v62, v63
	v_cvt_pk_bf16_f32 v59, v64, v65
	v_pk_add_f32 v[54:55], v[54:55], v[134:135]
	v_pk_add_f32 v[48:49], v[48:49], v[132:133]
	v_pk_add_f32 v[46:47], v[46:47], v[130:131]
	v_cvt_pk_bf16_f32 v60, v60, v61
	v_cvt_pk_bf16_f32 v61, v68, v69
	ds_bpermute_b32 v58, v253, v58
	ds_bpermute_b32 v59, v253, v59
	ds_bpermute_b32 v60, v253, v60
	ds_bpermute_b32 v61, v253, v61
	s_waitcnt lgkmcnt(0)
	global_store_dwordx4 v[66:67], v[58:61], off
	v_pk_add_f32 v[56:57], v[56:57], v[136:137]
	v_pk_mul_f32 v[54:55], v[150:151], v[54:55] op_sel_hi:[0,1]
	v_pk_mul_f32 v[58:59], v[150:151], v[48:49] op_sel_hi:[0,1]
	v_pk_mul_f32 v[48:49], v[150:151], v[46:47] op_sel_hi:[0,1]
	v_cvt_pk_bf16_f32 v46, v54, v55
	v_pk_mul_f32 v[56:57], v[150:151], v[56:57] op_sel_hi:[0,1]
	v_cvt_pk_bf16_f32 v47, v56, v57
	v_cvt_pk_bf16_f32 v48, v48, v49
	v_cvt_pk_bf16_f32 v49, v58, v59
	ds_bpermute_b32 v46, v253, v46
	ds_bpermute_b32 v47, v253, v47
	ds_bpermute_b32 v48, v253, v48
	ds_bpermute_b32 v49, v253, v49
	s_waitcnt lgkmcnt(0)
	global_store_dwordx4 v[66:67], v[46:49], off offset:256
	v_pk_add_f32 v[50:51], v[50:51], v[142:143]
	v_pk_add_f32 v[44:45], v[44:45], v[140:141]
	v_add_u32_e32 v46, 0x90, v192
	v_mad_i64_i32 v[46:47], s[40:41], v46, s76, v[158:159]
	v_pk_add_f32 v[48:49], v[52:53], v[144:145]
	v_pk_add_f32 v[42:43], v[42:43], v[138:139]
	v_lshl_add_u64 v[46:47], v[46:47], 0, v[160:161]
	v_pk_mul_f32 v[48:49], v[150:151], v[48:49] op_sel_hi:[0,1]
	v_pk_mul_f32 v[50:51], v[150:151], v[50:51] op_sel_hi:[0,1]
	v_pk_mul_f32 v[52:53], v[150:151], v[44:45] op_sel_hi:[0,1]
	v_pk_mul_f32 v[44:45], v[150:151], v[42:43] op_sel_hi:[0,1]
	v_cvt_pk_bf16_f32 v42, v50, v51
	v_cvt_pk_bf16_f32 v43, v48, v49
	v_pk_add_f32 v[30:31], v[30:31], v[134:135]
	v_pk_add_f32 v[16:17], v[16:17], v[132:133]
	v_pk_add_f32 v[14:15], v[14:15], v[130:131]
	v_cvt_pk_bf16_f32 v44, v44, v45
	v_cvt_pk_bf16_f32 v45, v52, v53
	ds_bpermute_b32 v42, v253, v42
	ds_bpermute_b32 v43, v253, v43
	ds_bpermute_b32 v44, v253, v44
	ds_bpermute_b32 v45, v253, v45
	s_waitcnt lgkmcnt(0)
	global_store_dwordx4 v[46:47], v[42:45], off
	v_pk_add_f32 v[32:33], v[32:33], v[136:137]
	v_pk_mul_f32 v[30:31], v[150:151], v[30:31] op_sel_hi:[0,1]
	v_pk_mul_f32 v[42:43], v[150:151], v[16:17] op_sel_hi:[0,1]
	v_pk_mul_f32 v[16:17], v[150:151], v[14:15] op_sel_hi:[0,1]
	v_cvt_pk_bf16_f32 v14, v30, v31
	v_pk_mul_f32 v[32:33], v[150:151], v[32:33] op_sel_hi:[0,1]
	v_cvt_pk_bf16_f32 v15, v32, v33
	v_cvt_pk_bf16_f32 v16, v16, v17
	v_cvt_pk_bf16_f32 v17, v42, v43
	ds_bpermute_b32 v14, v253, v14
	ds_bpermute_b32 v15, v253, v15
	ds_bpermute_b32 v16, v253, v16
	ds_bpermute_b32 v17, v253, v17
	s_waitcnt lgkmcnt(0)
	global_store_dwordx4 v[46:47], v[14:17], off offset:256
	v_pk_add_f32 v[12:13], v[12:13], v[140:141]
	v_pk_add_f32 v[10:11], v[10:11], v[138:139]
	v_add_u32_e32 v14, 0xa0, v192
	v_mad_i64_i32 v[14:15], s[40:41], v14, s76, v[158:159]
	v_pk_add_f32 v[16:17], v[20:21], v[144:145]
	v_pk_add_f32 v[18:19], v[18:19], v[142:143]
	v_pk_mul_f32 v[20:21], v[150:151], v[12:13] op_sel_hi:[0,1]
	v_pk_mul_f32 v[12:13], v[150:151], v[10:11] op_sel_hi:[0,1]
	v_lshl_add_u64 v[14:15], v[14:15], 0, v[160:161]
	v_pk_mul_f32 v[16:17], v[150:151], v[16:17] op_sel_hi:[0,1]
	v_pk_mul_f32 v[18:19], v[150:151], v[18:19] op_sel_hi:[0,1]
	v_cvt_pk_bf16_f32 v10, v18, v19
	v_cvt_pk_bf16_f32 v11, v16, v17
	v_cvt_pk_bf16_f32 v12, v12, v13
	v_cvt_pk_bf16_f32 v13, v20, v21
	ds_bpermute_b32 v10, v253, v10
	ds_bpermute_b32 v11, v253, v11
	ds_bpermute_b32 v12, v253, v12
	ds_bpermute_b32 v13, v253, v13
	s_waitcnt lgkmcnt(0)
	global_store_dwordx4 v[14:15], v[10:13], off
	v_pk_add_f32 v[18:19], v[34:35], v[130:131]
	v_pk_add_f32 v[4:5], v[4:5], v[140:141]
	v_pk_add_f32 v[10:11], v[40:41], v[136:137]
	v_pk_add_f32 v[12:13], v[38:39], v[134:135]
	v_pk_mul_f32 v[16:17], v[150:151], v[10:11] op_sel_hi:[0,1]
	v_pk_mul_f32 v[10:11], v[150:151], v[12:13] op_sel_hi:[0,1]
	v_pk_add_f32 v[12:13], v[36:37], v[132:133]
	v_cvt_pk_bf16_f32 v10, v10, v11
	v_cvt_pk_bf16_f32 v11, v16, v17
	v_pk_add_f32 v[2:3], v[2:3], v[138:139]
	v_pk_mul_f32 v[20:21], v[150:151], v[12:13] op_sel_hi:[0,1]
	v_pk_mul_f32 v[12:13], v[150:151], v[18:19] op_sel_hi:[0,1]
	v_cvt_pk_bf16_f32 v12, v12, v13
	v_cvt_pk_bf16_f32 v13, v20, v21
	ds_bpermute_b32 v10, v253, v10
	ds_bpermute_b32 v11, v253, v11
	ds_bpermute_b32 v12, v253, v12
	ds_bpermute_b32 v13, v253, v13
	s_waitcnt lgkmcnt(0)
	global_store_dwordx4 v[14:15], v[10:13], off offset:256
	v_pk_add_f32 v[8:9], v[8:9], v[144:145]
	v_pk_add_f32 v[6:7], v[6:7], v[142:143]
	v_add_u32_e32 v10, 0xb0, v192
	v_mad_i64_i32 v[10:11], s[40:41], v10, s76, v[158:159]
	v_pk_mul_f32 v[12:13], v[150:151], v[4:5] op_sel_hi:[0,1]
	v_pk_mul_f32 v[4:5], v[150:151], v[2:3] op_sel_hi:[0,1]
	v_lshl_add_u64 v[10:11], v[10:11], 0, v[160:161]
	v_pk_mul_f32 v[8:9], v[150:151], v[8:9] op_sel_hi:[0,1]
	v_pk_mul_f32 v[6:7], v[150:151], v[6:7] op_sel_hi:[0,1]
	v_cvt_pk_bf16_f32 v2, v6, v7
	v_cvt_pk_bf16_f32 v3, v8, v9
	v_cvt_pk_bf16_f32 v4, v4, v5
	v_cvt_pk_bf16_f32 v5, v12, v13
	ds_bpermute_b32 v2, v253, v2
	ds_bpermute_b32 v3, v253, v3
	ds_bpermute_b32 v4, v253, v4
	ds_bpermute_b32 v5, v253, v5
	s_waitcnt lgkmcnt(0)
	global_store_dwordx4 v[10:11], v[2:5], off
	v_pk_add_f32 v[8:9], v[22:23], v[130:131]
	s_cmp_lg_u32 s10, s52
	v_pk_add_f32 v[2:3], v[28:29], v[136:137]
	v_pk_add_f32 v[4:5], v[26:27], v[134:135]
	v_pk_mul_f32 v[6:7], v[150:151], v[2:3] op_sel_hi:[0,1]
	v_pk_mul_f32 v[2:3], v[150:151], v[4:5] op_sel_hi:[0,1]
	v_pk_add_f32 v[4:5], v[24:25], v[132:133]
	v_cvt_pk_bf16_f32 v2, v2, v3
	v_cvt_pk_bf16_f32 v3, v6, v7
	s_nop 0
	v_pk_mul_f32 v[12:13], v[150:151], v[4:5] op_sel_hi:[0,1]
	v_pk_mul_f32 v[4:5], v[150:151], v[8:9] op_sel_hi:[0,1]
	v_cvt_pk_bf16_f32 v4, v4, v5
	v_cvt_pk_bf16_f32 v5, v12, v13
	ds_bpermute_b32 v2, v253, v2
	ds_bpermute_b32 v3, v253, v3
	ds_bpermute_b32 v4, v253, v4
	ds_bpermute_b32 v5, v253, v5
	s_waitcnt lgkmcnt(0)
	global_store_dwordx4 v[10:11], v[2:5], off offset:256
	s_cbranch_scc1 .LBB0_192
	s_nop 0
	v_mov_b32_e32 v2, v0
	s_mov_b32 s40, 15
	s_andn2_b64 vcc, exec, s[14:15]
	s_cbranch_vccnz .LBB0_192
	v_writelane_b32 v255, 2, 5
	v_writelane_b32 v255, 16, 6
	s_branch .Lmy_cvgu

.LBB0_777:
	v_mbcnt_lo_u32_b32 v254, -1, 0
	v_mbcnt_hi_u32_b32 v254, -1, v254
	v_lshrrev_b32_e32 v253, 2, v254
	v_add_u32_e32 v253, v253, v151
	v_and_b32_e32 v254, 15, v254
	v_sub_u32_e32 v253, v253, v254
	v_lshl_add_u32 v142, s64, 8, v253
	v_mbcnt_lo_u32_b32 v254, -1, 0
	v_mbcnt_hi_u32_b32 v254, -1, v254
	v_lshrrev_b32_e32 v253, 4, v254
	v_lshlrev_b32_e32 v253, 3, v253
	v_sub_u32_e32 v253, v168, v253
	v_and_b32_e32 v254, 3, v254
	v_lshl_add_u32 v253, v254, 3, v253
	v_lshl_or_b32 v140, s65, 8, v253
	v_mbcnt_lo_u32_b32 v254, -1, 0
	v_mbcnt_hi_u32_b32 v254, -1, v254
	v_lshrrev_b32_e32 v253, 2, v254
	v_lshlrev_b32_e32 v253, 2, v253
	v_and_b32_e32 v254, 3, v254
	v_lshl_or_b32 v253, v254, 6, v253
	v_ashrrev_i32_e32 v143, 31, v142
	v_ashrrev_i32_e32 v141, 31, v140
	v_lshlrev_b64 v[144:145], 12, v[142:143]
	v_lshl_add_u64 v[144:145], s[14:15], 0, v[144:145]
	v_lshlrev_b64 v[146:147], 1, v[140:141]
	v_lshl_add_u64 v[140:141], v[144:145], 0, v[146:147]
	v_cvt_pk_bf16_f32 v126, v126, v127
	v_cvt_pk_bf16_f32 v127, v128, v129
	v_cvt_pk_bf16_f32 v128, v122, v123
	v_cvt_pk_bf16_f32 v129, v124, v125
	ds_bpermute_b32 v126, v253, v126
	ds_bpermute_b32 v127, v253, v127
	ds_bpermute_b32 v128, v253, v128
	ds_bpermute_b32 v129, v253, v129
	s_waitcnt lgkmcnt(0)
	global_store_dwordx4 v[140:141], v[126:129], off
	v_cvt_pk_bf16_f32 v114, v114, v115
	v_cvt_pk_bf16_f32 v115, v116, v117
	v_cvt_pk_bf16_f32 v116, v106, v107
	v_or_b32_e32 v106, 16, v142
	v_ashrrev_i32_e32 v107, 31, v106
	v_lshlrev_b64 v[106:107], 12, v[106:107]
	v_lshl_add_u64 v[106:107], s[14:15], 0, v[106:107]
	v_cvt_pk_bf16_f32 v117, v108, v109
	ds_bpermute_b32 v114, v253, v114
	ds_bpermute_b32 v115, v253, v115
	ds_bpermute_b32 v116, v253, v116
	ds_bpermute_b32 v117, v253, v117
	s_waitcnt lgkmcnt(0)
	global_store_dwordx4 v[140:141], v[114:117], off offset:256
	s_nop 1
	v_lshl_add_u64 v[114:115], v[106:107], 0, v[146:147]
	v_cvt_pk_bf16_f32 v106, v118, v119
	v_cvt_pk_bf16_f32 v107, v120, v121
	v_cvt_pk_bf16_f32 v108, v110, v111
	v_cvt_pk_bf16_f32 v109, v112, v113
	ds_bpermute_b32 v106, v253, v106
	ds_bpermute_b32 v107, v253, v107
	ds_bpermute_b32 v108, v253, v108
	ds_bpermute_b32 v109, v253, v109
	s_waitcnt lgkmcnt(0)
	global_store_dwordx4 v[114:115], v[106:109], off
	v_cvt_pk_bf16_f32 v98, v98, v99
	v_cvt_pk_bf16_f32 v99, v100, v101
	v_cvt_pk_bf16_f32 v100, v90, v91
	v_or_b32_e32 v90, 32, v142
	v_ashrrev_i32_e32 v91, 31, v90
	v_lshlrev_b64 v[90:91], 12, v[90:91]
	v_lshl_add_u64 v[90:91], s[14:15], 0, v[90:91]
	v_cvt_pk_bf16_f32 v101, v92, v93
	ds_bpermute_b32 v98, v253, v98
	ds_bpermute_b32 v99, v253, v99
	ds_bpermute_b32 v100, v253, v100
	ds_bpermute_b32 v101, v253, v101
	s_waitcnt lgkmcnt(0)
	global_store_dwordx4 v[114:115], v[98:101], off offset:256
	s_nop 1
	v_lshl_add_u64 v[98:99], v[90:91], 0, v[146:147]
	v_cvt_pk_bf16_f32 v90, v102, v103
	v_cvt_pk_bf16_f32 v91, v104, v105
	v_cvt_pk_bf16_f32 v92, v94, v95
	v_cvt_pk_bf16_f32 v93, v96, v97
	ds_bpermute_b32 v90, v253, v90
	ds_bpermute_b32 v91, v253, v91
	ds_bpermute_b32 v92, v253, v92
	ds_bpermute_b32 v93, v253, v93
	s_waitcnt lgkmcnt(0)
	global_store_dwordx4 v[98:99], v[90:93], off
	v_cvt_pk_bf16_f32 v82, v82, v83
	v_cvt_pk_bf16_f32 v83, v84, v85
	v_cvt_pk_bf16_f32 v84, v74, v75
	v_or_b32_e32 v74, 48, v142
	v_ashrrev_i32_e32 v75, 31, v74
	v_lshlrev_b64 v[74:75], 12, v[74:75]
	v_lshl_add_u64 v[74:75], s[14:15], 0, v[74:75]
	v_cvt_pk_bf16_f32 v85, v76, v77
	ds_bpermute_b32 v82, v253, v82
	ds_bpermute_b32 v83, v253, v83
	ds_bpermute_b32 v84, v253, v84
	ds_bpermute_b32 v85, v253, v85
	s_waitcnt lgkmcnt(0)
	global_store_dwordx4 v[98:99], v[82:85], off offset:256
	s_nop 1
	v_lshl_add_u64 v[82:83], v[74:75], 0, v[146:147]
	v_cvt_pk_bf16_f32 v74, v86, v87
	v_cvt_pk_bf16_f32 v75, v88, v89
	v_cvt_pk_bf16_f32 v76, v78, v79
	v_cvt_pk_bf16_f32 v77, v80, v81
	ds_bpermute_b32 v74, v253, v74
	ds_bpermute_b32 v75, v253, v75
	ds_bpermute_b32 v76, v253, v76
	ds_bpermute_b32 v77, v253, v77
	s_waitcnt lgkmcnt(0)
	global_store_dwordx4 v[82:83], v[74:77], off
	v_cvt_pk_bf16_f32 v70, v70, v71
	v_cvt_pk_bf16_f32 v71, v72, v73
	v_cvt_pk_bf16_f32 v72, v66, v67
	v_cvt_pk_bf16_f32 v73, v68, v69
	ds_bpermute_b32 v70, v253, v70
	ds_bpermute_b32 v71, v253, v71
	ds_bpermute_b32 v72, v253, v72
	ds_bpermute_b32 v73, v253, v73
	s_waitcnt lgkmcnt(0)
	global_store_dwordx4 v[82:83], v[70:73], off offset:256
	v_cvt_pk_bf16_f32 v62, v62, v63
	v_cvt_pk_bf16_f32 v63, v64, v65
	v_cvt_pk_bf16_f32 v64, v58, v59
	v_add_co_u32_e32 v58, vcc, s50, v140
	v_lshl_add_u64 v[66:67], v[140:141], 0, s[10:11]
	s_nop 0
	v_addc_co_u32_e32 v59, vcc, 0, v141, vcc
	v_cvt_pk_bf16_f32 v65, v60, v61
	ds_bpermute_b32 v62, v253, v62
	ds_bpermute_b32 v63, v253, v63
	ds_bpermute_b32 v64, v253, v64
	ds_bpermute_b32 v65, v253, v65
	s_waitcnt lgkmcnt(0)
	global_store_dwordx4 v[58:59], v[62:65], off
	v_cvt_pk_bf16_f32 v42, v42, v43
	v_cvt_pk_bf16_f32 v43, v44, v45
	v_cvt_pk_bf16_f32 v44, v30, v31
	v_cvt_pk_bf16_f32 v45, v32, v33
	ds_bpermute_b32 v42, v253, v42
	ds_bpermute_b32 v43, v253, v43
	ds_bpermute_b32 v44, v253, v44
	ds_bpermute_b32 v45, v253, v45
	s_waitcnt lgkmcnt(0)
	global_store_dwordx4 v[66:67], v[42:45], off offset:256
	v_cvt_pk_bf16_f32 v30, v46, v47
	v_cvt_pk_bf16_f32 v31, v48, v49
	v_cvt_pk_bf16_f32 v32, v38, v39
	v_add_co_u32_e32 v38, vcc, s59, v140
	s_nop 0
	v_lshl_add_u64 v[42:43], v[140:141], 0, s[34:35]
	v_addc_co_u32_e32 v39, vcc, 0, v141, vcc
	v_cvt_pk_bf16_f32 v33, v40, v41
	ds_bpermute_b32 v30, v253, v30
	ds_bpermute_b32 v31, v253, v31
	ds_bpermute_b32 v32, v253, v32
	ds_bpermute_b32 v33, v253, v33
	s_waitcnt lgkmcnt(0)
	global_store_dwordx4 v[38:39], v[30:33], off
	v_cvt_pk_bf16_f32 v18, v18, v19
	v_cvt_pk_bf16_f32 v19, v20, v21
	v_cvt_pk_bf16_f32 v20, v10, v11
	v_cvt_pk_bf16_f32 v21, v12, v13
	ds_bpermute_b32 v18, v253, v18
	ds_bpermute_b32 v19, v253, v19
	ds_bpermute_b32 v20, v253, v20
	ds_bpermute_b32 v21, v253, v21
	s_waitcnt lgkmcnt(0)
	global_store_dwordx4 v[42:43], v[18:21], off offset:256
	v_cvt_pk_bf16_f32 v10, v22, v23
	v_cvt_pk_bf16_f32 v11, v24, v25
	v_cvt_pk_bf16_f32 v12, v14, v15
	v_add_co_u32_e32 v14, vcc, s60, v140
	s_nop 0
	v_lshl_add_u64 v[18:19], v[140:141], 0, s[36:37]
	v_cvt_pk_bf16_f32 v13, v16, v17
	v_addc_co_u32_e32 v15, vcc, 0, v141, vcc
	ds_bpermute_b32 v10, v253, v10
	ds_bpermute_b32 v11, v253, v11
	ds_bpermute_b32 v12, v253, v12
	ds_bpermute_b32 v13, v253, v13
	s_waitcnt lgkmcnt(0)
	global_store_dwordx4 v[14:15], v[10:13], off
	s_nop 1
	v_cvt_pk_bf16_f32 v10, v54, v55
	v_cvt_pk_bf16_f32 v11, v56, v57
	v_cvt_pk_bf16_f32 v12, v50, v51
	v_cvt_pk_bf16_f32 v13, v52, v53
	ds_bpermute_b32 v10, v253, v10
	ds_bpermute_b32 v11, v253, v11
	ds_bpermute_b32 v12, v253, v12
	ds_bpermute_b32 v13, v253, v13
	s_waitcnt lgkmcnt(0)
	global_store_dwordx4 v[18:19], v[10:13], off offset:256
	v_cvt_pk_bf16_f32 v6, v6, v7
	v_cvt_pk_bf16_f32 v7, v8, v9
	v_cvt_pk_bf16_f32 v8, v2, v3
	v_add_co_u32_e32 v2, vcc, s62, v140
	s_nop 0
	v_lshl_add_u64 v[10:11], v[140:141], 0, s[38:39]
	v_addc_co_u32_e32 v3, vcc, 0, v141, vcc
	s_and_b64 vcc, exec, s[2:3]
	s_mov_b64 s[2:3], -1
	v_cvt_pk_bf16_f32 v9, v4, v5
	ds_bpermute_b32 v6, v253, v6
	ds_bpermute_b32 v7, v253, v7
	ds_bpermute_b32 v8, v253, v8
	ds_bpermute_b32 v9, v253, v9
	s_waitcnt lgkmcnt(0)
	global_store_dwordx4 v[2:3], v[6:9], off
	v_cvt_pk_bf16_f32 v2, v34, v35
	v_cvt_pk_bf16_f32 v3, v36, v37
	v_cvt_pk_bf16_f32 v4, v26, v27
	v_cvt_pk_bf16_f32 v5, v28, v29
	ds_bpermute_b32 v2, v253, v2
	ds_bpermute_b32 v3, v253, v3
	ds_bpermute_b32 v4, v253, v4
	ds_bpermute_b32 v5, v253, v5
	s_waitcnt lgkmcnt(0)
	global_store_dwordx4 v[10:11], v[2:5], off offset:256
	s_cbranch_vccnz .LBB0_764
	s_andn2_b64 vcc, exec, s[12:13]
	s_cbranch_vccnz .LBB0_763
	s_barrier
	s_branch .LBB0_763
